# speedup vs baseline: 1.0030x; 1.0030x over previous
.Lq2_nd0_0:
	v_mfma_scale_f32_32x32x64_f8f6f4 v[18:33], v[66:73], v[106:113], 0, v203, v203 op_sel_hi:[0,0,0]
	v_exp_f32_e64 v2, -v2
	v_exp_f32_e64 v3, -v3
	v_exp_f32_e64 v4, -v4
	v_exp_f32_e64 v5, -v5
	s_waitcnt lgkmcnt(0)
	v_add_co_u32_e64 v200, s[42:43], v200, v200
	v_add_co_u32_e64 v200, s[48:49], v200, v200
	v_add_co_u32_e64 v200, s[50:51], v200, v200
	v_add_co_u32_e64 v200, s[56:57], v200, v200
	v_pk_add_f32 v[2:3], v[2:3], v[162:163]
	v_pk_add_f32 v[4:5], v[4:5], v[164:165]
	v_cndmask_b32_e64 v204, 1.0, v2, s[42:43]
	v_cndmask_b32_e64 v205, 1.0, v3, s[48:49]
	v_cndmask_b32_e64 v206, 1.0, v4, s[50:51]
	v_cndmask_b32_e64 v207, 1.0, v5, s[56:57]
	v_mfma_scale_f32_32x32x64_f8f6f4 v[18:33], v[74:81], v[122:129], v[18:33], v203, v203 op_sel_hi:[0,0,0]
	v_exp_f32_e64 v6, -v6
	v_exp_f32_e64 v7, -v7
	v_exp_f32_e64 v8, -v8
	v_exp_f32_e64 v9, -v9
	v_add_co_u32_e64 v200, s[42:43], v200, v200
	v_add_co_u32_e64 v200, s[48:49], v200, v200
	v_add_co_u32_e64 v200, s[50:51], v200, v200
	v_add_co_u32_e64 v200, s[56:57], v200, v200
	v_pk_add_f32 v[6:7], v[6:7], v[166:167]
	v_pk_add_f32 v[8:9], v[8:9], v[168:169]
	v_cndmask_b32_e64 v208, 1.0, v6, s[42:43]
	v_cndmask_b32_e64 v209, 1.0, v7, s[48:49]
	v_cndmask_b32_e64 v210, 1.0, v8, s[50:51]
	v_cndmask_b32_e64 v211, 1.0, v9, s[56:57]
	v_mfma_scale_f32_32x32x64_f8f6f4 v[18:33], v[82:89], v[114:121], v[18:33], v203, v203 op_sel_hi:[0,0,0]
	v_exp_f32_e64 v10, -v10
	v_exp_f32_e64 v11, -v11
	v_exp_f32_e64 v12, -v12
	v_exp_f32_e64 v13, -v13
	v_add_co_u32_e64 v200, s[42:43], v200, v200
	v_add_co_u32_e64 v200, s[48:49], v200, v200
	v_add_co_u32_e64 v200, s[50:51], v200, v200
	v_add_co_u32_e64 v200, s[56:57], v200, v200
	v_pk_add_f32 v[10:11], v[10:11], v[170:171]
	v_pk_add_f32 v[12:13], v[12:13], v[172:173]
	v_cndmask_b32_e64 v212, 1.0, v10, s[42:43]
	v_cndmask_b32_e64 v213, 1.0, v11, s[48:49]
	v_cndmask_b32_e64 v214, 1.0, v12, s[50:51]
	v_cndmask_b32_e64 v215, 1.0, v13, s[56:57]
	v_mfma_scale_f32_32x32x64_f8f6f4 v[18:33], v[90:97], v[98:105], v[18:33], v203, v203 op_sel_hi:[0,0,0]
	v_exp_f32_e64 v14, -v14
	v_exp_f32_e64 v15, -v15
	v_exp_f32_e64 v16, -v16
	v_exp_f32_e64 v17, -v17
	v_add_co_u32_e64 v200, s[42:43], v200, v200
	v_add_co_u32_e64 v200, s[48:49], v200, v200
	v_add_co_u32_e64 v200, s[50:51], v200, v200
	v_add_co_u32_e64 v200, s[56:57], v200, v200
	v_pk_add_f32 v[14:15], v[14:15], v[174:175]
	v_pk_add_f32 v[16:17], v[16:17], v[176:177]
	v_cndmask_b32_e64 v216, 1.0, v14, s[42:43]
	v_cndmask_b32_e64 v217, 1.0, v15, s[48:49]
	v_cndmask_b32_e64 v218, 1.0, v16, s[50:51]
	v_cndmask_b32_e64 v219, 1.0, v17, s[56:57]
	s_cmp_lg_u32 s55, s40
	s_cbranch_scc1 .Lq2_nd1_0
	s_nop 15
	s_nop 7
	v_cndmask_b32_e64 v18, v18, v199, s[0:1]
	v_cndmask_b32_e64 v19, v19, v199, s[2:3]
	v_cndmask_b32_e64 v20, v20, v199, s[4:5]
	v_cndmask_b32_e64 v21, v21, v199, s[6:7]
	v_cndmask_b32_e64 v22, v22, v199, s[8:9]
	v_cndmask_b32_e64 v23, v23, v199, s[10:11]
	v_cndmask_b32_e64 v24, v24, v199, s[12:13]
	v_cndmask_b32_e64 v25, v25, v199, s[14:15]
	v_cndmask_b32_e64 v26, v26, v199, s[16:17]
	v_cndmask_b32_e64 v27, v27, v199, s[18:19]
	v_cndmask_b32_e64 v28, v28, v199, s[20:21]
	v_cndmask_b32_e64 v29, v29, v199, s[22:23]
	v_cndmask_b32_e64 v30, v30, v199, s[24:25]
	v_cndmask_b32_e64 v31, v31, v199, s[26:27]
	v_cndmask_b32_e64 v32, v32, v199, s[28:29]
	v_cndmask_b32_e64 v33, v33, v199, s[30:31]
.Lq2_nd1_0:
	s_nop 3
	s_waitcnt vmcnt(6)
	v_mfma_scale_f32_32x32x64_f8f6f4 v[2:17], v[34:41], v[146:153], 0, v203, v203 op_sel_hi:[0,0,0]
	v_exp_f32_e64 v18, -v18
	v_exp_f32_e64 v19, -v19
	v_exp_f32_e64 v20, -v20
	v_exp_f32_e64 v21, -v21
	v_add_co_u32_e64 v200, s[42:43], v200, v200
	v_add_co_u32_e64 v200, s[48:49], v200, v200
	v_add_co_u32_e64 v200, s[50:51], v200, v200
	v_add_co_u32_e64 v200, s[56:57], v200, v200
	v_pk_add_f32 v[18:19], v[18:19], v[178:179]
	v_pk_add_f32 v[20:21], v[20:21], v[180:181]
	v_cndmask_b32_e64 v220, 1.0, v18, s[42:43]
	v_cndmask_b32_e64 v221, 1.0, v19, s[48:49]
	v_cndmask_b32_e64 v222, 1.0, v20, s[50:51]
	v_cndmask_b32_e64 v223, 1.0, v21, s[56:57]
	s_waitcnt vmcnt(4)
	v_mfma_scale_f32_32x32x64_f8f6f4 v[2:17], v[42:49], v[154:161], v[2:17], v203, v203 op_sel_hi:[0,0,0]
	v_exp_f32_e64 v22, -v22
	v_exp_f32_e64 v23, -v23
	v_exp_f32_e64 v24, -v24
	v_exp_f32_e64 v25, -v25
	v_add_co_u32_e64 v200, s[42:43], v200, v200
	v_add_co_u32_e64 v200, s[48:49], v200, v200
	v_add_co_u32_e64 v200, s[50:51], v200, v200
	v_add_co_u32_e64 v200, s[56:57], v200, v200
	v_pk_add_f32 v[22:23], v[22:23], v[182:183]
	v_pk_add_f32 v[24:25], v[24:25], v[184:185]
	v_cndmask_b32_e64 v224, 1.0, v22, s[42:43]
	v_cndmask_b32_e64 v225, 1.0, v23, s[48:49]
	v_cndmask_b32_e64 v226, 1.0, v24, s[50:51]
	v_cndmask_b32_e64 v227, 1.0, v25, s[56:57]
	s_waitcnt vmcnt(2)
	v_mfma_scale_f32_32x32x64_f8f6f4 v[2:17], v[50:57], v[138:145], v[2:17], v203, v203 op_sel_hi:[0,0,0]
	v_exp_f32_e64 v26, -v26
	v_exp_f32_e64 v27, -v27
	v_exp_f32_e64 v28, -v28
	v_exp_f32_e64 v29, -v29
	v_add_co_u32_e64 v200, s[42:43], v200, v200
	v_add_co_u32_e64 v200, s[48:49], v200, v200
	v_add_co_u32_e64 v200, s[50:51], v200, v200
	v_add_co_u32_e64 v200, s[56:57], v200, v200
	v_pk_add_f32 v[26:27], v[26:27], v[186:187]
	v_pk_add_f32 v[28:29], v[28:29], v[188:189]
	v_cndmask_b32_e64 v228, 1.0, v26, s[42:43]
	v_cndmask_b32_e64 v229, 1.0, v27, s[48:49]
	v_cndmask_b32_e64 v230, 1.0, v28, s[50:51]
	v_cndmask_b32_e64 v231, 1.0, v29, s[56:57]
	s_waitcnt vmcnt(0)
	v_mfma_scale_f32_32x32x64_f8f6f4 v[2:17], v[58:65], v[130:137], v[2:17], v203, v203 op_sel_hi:[0,0,0]
	v_exp_f32_e64 v30, -v30
	v_exp_f32_e64 v31, -v31
	v_exp_f32_e64 v32, -v32
	v_exp_f32_e64 v33, -v33
	v_add_co_u32_e64 v200, s[42:43], v200, v200
	v_add_co_u32_e64 v200, s[48:49], v200, v200
	v_add_co_u32_e64 v200, s[50:51], v200, v200
	v_add_co_u32_e64 v200, s[56:57], v200, v200
	v_pk_add_f32 v[30:31], v[30:31], v[190:191]
	v_pk_add_f32 v[32:33], v[32:33], v[192:193]
	v_cndmask_b32_e64 v232, 1.0, v30, s[42:43]
	v_cndmask_b32_e64 v233, 1.0, v31, s[48:49]
	v_cndmask_b32_e64 v234, 1.0, v32, s[50:51]
	v_cndmask_b32_e64 v235, 1.0, v33, s[56:57]
	s_lshl_b32 s34, s39, 2
	s_add_i32 s34, s34, 1
	s_add_i32 s34, s34, s35
	s_and_b32 s41, s34, 15
	s_add_i32 s54, s34, 1
	s_and_b32 s54, s54, 15
	s_lshl_b32 s55, s41, 8
	s_lshl_b32 s38, s52, 12
	s_add_i32 s55, s55, s38
	v_lshl_add_u32 v236, v194, 2, s55
	ds_read_b32 v200, v236
	s_lshl_b32 s34, s54, 3
	s_add_i32 s34, s34, s52
	s_lshl_b32 s34, s34, 13
	s_add_i32 s34, s34, s53
	buffer_load_dwordx4 v[106:109], v195, s[44:47], s34 offen
	s_or_b32 s42, s34, 0x400
	buffer_load_dwordx4 v[110:113], v195, s[44:47], s42 offen
	s_or_b32 s43, s34, 0x800
	buffer_load_dwordx4 v[122:125], v195, s[44:47], s43 offen
	s_or_b32 s42, s34, 0xc00
	buffer_load_dwordx4 v[126:129], v195, s[44:47], s42 offen
	s_or_b32 s43, s34, 0x1000
	buffer_load_dwordx4 v[114:117], v195, s[44:47], s43 offen
	s_or_b32 s42, s34, 0x1400
	buffer_load_dwordx4 v[118:121], v195, s[44:47], s42 offen
	s_or_b32 s43, s34, 0x1800
	buffer_load_dwordx4 v[98:101], v195, s[44:47], s43 offen
	s_or_b32 s42, s34, 0x1c00
	buffer_load_dwordx4 v[102:105], v195, s[44:47], s42 offen
	s_lshl_b32 s55, s41, 3
	s_add_i32 s55, s55, s52
	s_cmp_lg_u32 s55, s33
	s_cbranch_scc1 .Lq2_nd0_1
	v_cndmask_b32_e64 v2, v2, v198, s[0:1]
	v_cndmask_b32_e64 v3, v3, v198, s[2:3]
	v_cndmask_b32_e64 v4, v4, v198, s[4:5]
	v_cndmask_b32_e64 v5, v5, v198, s[6:7]
	v_cndmask_b32_e64 v6, v6, v198, s[8:9]
	v_cndmask_b32_e64 v7, v7, v198, s[10:11]
	v_cndmask_b32_e64 v8, v8, v198, s[12:13]
	v_cndmask_b32_e64 v9, v9, v198, s[14:15]
	v_cndmask_b32_e64 v10, v10, v198, s[16:17]
	v_cndmask_b32_e64 v11, v11, v198, s[18:19]
	v_cndmask_b32_e64 v12, v12, v198, s[20:21]
	v_cndmask_b32_e64 v13, v13, v198, s[22:23]
	v_cndmask_b32_e64 v14, v14, v198, s[24:25]
	v_cndmask_b32_e64 v15, v15, v198, s[26:27]
	v_cndmask_b32_e64 v16, v16, v198, s[28:29]
	v_cndmask_b32_e64 v17, v17, v198, s[30:31]
.Lq2_nd0_1:
	v_mfma_scale_f32_32x32x64_f8f6f4 v[18:33], v[66:73], v[146:153], 0, v203, v203 op_sel_hi:[0,0,0]
	v_exp_f32_e64 v2, -v2
	v_exp_f32_e64 v3, -v3
	v_exp_f32_e64 v4, -v4
	v_exp_f32_e64 v5, -v5
	s_waitcnt lgkmcnt(0)
	v_add_co_u32_e64 v200, s[42:43], v200, v200
	v_add_co_u32_e64 v200, s[48:49], v200, v200
	v_add_co_u32_e64 v200, s[50:51], v200, v200
	v_add_co_u32_e64 v200, s[56:57], v200, v200
	v_pk_add_f32 v[2:3], v[2:3], v[162:163]
	v_pk_add_f32 v[4:5], v[4:5], v[164:165]
	s_mov_b64 exec, s[42:43]
	v_mul_f32_e32 v204, v204, v2
	s_mov_b64 exec, s[48:49]
	v_mul_f32_e32 v205, v205, v3
	s_mov_b64 exec, s[50:51]
	v_mul_f32_e32 v206, v206, v4
	s_mov_b64 exec, s[56:57]
	v_mul_f32_e32 v207, v207, v5
	s_mov_b64 exec, -1
	s_nop 1
	v_mfma_scale_f32_32x32x64_f8f6f4 v[18:33], v[74:81], v[154:161], v[18:33], v203, v203 op_sel_hi:[0,0,0]
	v_exp_f32_e64 v6, -v6
	v_exp_f32_e64 v7, -v7
	v_exp_f32_e64 v8, -v8
	v_exp_f32_e64 v9, -v9
	v_add_co_u32_e64 v200, s[42:43], v200, v200
	v_add_co_u32_e64 v200, s[48:49], v200, v200
	v_add_co_u32_e64 v200, s[50:51], v200, v200
	v_add_co_u32_e64 v200, s[56:57], v200, v200
	v_pk_add_f32 v[6:7], v[6:7], v[166:167]
	v_pk_add_f32 v[8:9], v[8:9], v[168:169]
	s_mov_b64 exec, s[42:43]
	v_mul_f32_e32 v208, v208, v6
	s_mov_b64 exec, s[48:49]
	v_mul_f32_e32 v209, v209, v7
	s_mov_b64 exec, s[50:51]
	v_mul_f32_e32 v210, v210, v8
	s_mov_b64 exec, s[56:57]
	v_mul_f32_e32 v211, v211, v9
	s_mov_b64 exec, -1
	s_nop 1
	v_mfma_scale_f32_32x32x64_f8f6f4 v[18:33], v[82:89], v[138:145], v[18:33], v203, v203 op_sel_hi:[0,0,0]
	v_exp_f32_e64 v10, -v10
	v_exp_f32_e64 v11, -v11
	v_exp_f32_e64 v12, -v12
	v_exp_f32_e64 v13, -v13
	v_add_co_u32_e64 v200, s[42:43], v200, v200
	v_add_co_u32_e64 v200, s[48:49], v200, v200
	v_add_co_u32_e64 v200, s[50:51], v200, v200
	v_add_co_u32_e64 v200, s[56:57], v200, v200
	v_pk_add_f32 v[10:11], v[10:11], v[170:171]
	v_pk_add_f32 v[12:13], v[12:13], v[172:173]
	s_mov_b64 exec, s[42:43]
	v_mul_f32_e32 v212, v212, v10
	s_mov_b64 exec, s[48:49]
	v_mul_f32_e32 v213, v213, v11
	s_mov_b64 exec, s[50:51]
	v_mul_f32_e32 v214, v214, v12
	s_mov_b64 exec, s[56:57]
	v_mul_f32_e32 v215, v215, v13
	s_mov_b64 exec, -1
	s_nop 1
	v_mfma_scale_f32_32x32x64_f8f6f4 v[18:33], v[90:97], v[130:137], v[18:33], v203, v203 op_sel_hi:[0,0,0]
	v_exp_f32_e64 v14, -v14
	v_exp_f32_e64 v15, -v15
	v_exp_f32_e64 v16, -v16
	v_exp_f32_e64 v17, -v17
	v_add_co_u32_e64 v200, s[42:43], v200, v200
	v_add_co_u32_e64 v200, s[48:49], v200, v200
	v_add_co_u32_e64 v200, s[50:51], v200, v200
	v_add_co_u32_e64 v200, s[56:57], v200, v200
	v_pk_add_f32 v[14:15], v[14:15], v[174:175]
	v_pk_add_f32 v[16:17], v[16:17], v[176:177]
	s_mov_b64 exec, s[42:43]
	v_mul_f32_e32 v216, v216, v14
	s_mov_b64 exec, s[48:49]
	v_mul_f32_e32 v217, v217, v15
	s_mov_b64 exec, s[50:51]
	v_mul_f32_e32 v218, v218, v16
	s_mov_b64 exec, s[56:57]
	v_mul_f32_e32 v219, v219, v17
	s_mov_b64 exec, -1
	s_nop 1
	s_cmp_lg_u32 s55, s40
	s_cbranch_scc1 .Lq2_nd1_1
	s_nop 15
	s_nop 7
	v_cndmask_b32_e64 v18, v18, v199, s[0:1]
	v_cndmask_b32_e64 v19, v19, v199, s[2:3]
	v_cndmask_b32_e64 v20, v20, v199, s[4:5]
	v_cndmask_b32_e64 v21, v21, v199, s[6:7]
	v_cndmask_b32_e64 v22, v22, v199, s[8:9]
	v_cndmask_b32_e64 v23, v23, v199, s[10:11]
	v_cndmask_b32_e64 v24, v24, v199, s[12:13]
	v_cndmask_b32_e64 v25, v25, v199, s[14:15]
	v_cndmask_b32_e64 v26, v26, v199, s[16:17]
	v_cndmask_b32_e64 v27, v27, v199, s[18:19]
	v_cndmask_b32_e64 v28, v28, v199, s[20:21]
	v_cndmask_b32_e64 v29, v29, v199, s[22:23]
	v_cndmask_b32_e64 v30, v30, v199, s[24:25]
	v_cndmask_b32_e64 v31, v31, v199, s[26:27]
	v_cndmask_b32_e64 v32, v32, v199, s[28:29]
	v_cndmask_b32_e64 v33, v33, v199, s[30:31]
.Lq2_nd1_1:
	s_nop 3
	s_waitcnt vmcnt(6)
	v_mfma_scale_f32_32x32x64_f8f6f4 v[2:17], v[34:41], v[106:113], 0, v203, v203 op_sel_hi:[0,0,0]
	v_exp_f32_e64 v18, -v18
	v_exp_f32_e64 v19, -v19
	v_exp_f32_e64 v20, -v20
	v_exp_f32_e64 v21, -v21
	v_add_co_u32_e64 v200, s[42:43], v200, v200
	v_add_co_u32_e64 v200, s[48:49], v200, v200
	v_add_co_u32_e64 v200, s[50:51], v200, v200
	v_add_co_u32_e64 v200, s[56:57], v200, v200
	v_pk_add_f32 v[18:19], v[18:19], v[178:179]
	v_pk_add_f32 v[20:21], v[20:21], v[180:181]
	s_mov_b64 exec, s[42:43]
	v_mul_f32_e32 v220, v220, v18
	s_mov_b64 exec, s[48:49]
	v_mul_f32_e32 v221, v221, v19
	s_mov_b64 exec, s[50:51]
	v_mul_f32_e32 v222, v222, v20
	s_mov_b64 exec, s[56:57]
	v_mul_f32_e32 v223, v223, v21
	s_mov_b64 exec, -1
	s_nop 1
	s_waitcnt vmcnt(4)
	v_mfma_scale_f32_32x32x64_f8f6f4 v[2:17], v[42:49], v[122:129], v[2:17], v203, v203 op_sel_hi:[0,0,0]
	v_exp_f32_e64 v22, -v22
	v_exp_f32_e64 v23, -v23
	v_exp_f32_e64 v24, -v24
	v_exp_f32_e64 v25, -v25
	v_add_co_u32_e64 v200, s[42:43], v200, v200
	v_add_co_u32_e64 v200, s[48:49], v200, v200
	v_add_co_u32_e64 v200, s[50:51], v200, v200
	v_add_co_u32_e64 v200, s[56:57], v200, v200
	v_pk_add_f32 v[22:23], v[22:23], v[182:183]
	v_pk_add_f32 v[24:25], v[24:25], v[184:185]
	s_mov_b64 exec, s[42:43]
	v_mul_f32_e32 v224, v224, v22
	s_mov_b64 exec, s[48:49]
	v_mul_f32_e32 v225, v225, v23
	s_mov_b64 exec, s[50:51]
	v_mul_f32_e32 v226, v226, v24
	s_mov_b64 exec, s[56:57]
	v_mul_f32_e32 v227, v227, v25
	s_mov_b64 exec, -1
	s_nop 1
	s_waitcnt vmcnt(2)
	v_mfma_scale_f32_32x32x64_f8f6f4 v[2:17], v[50:57], v[114:121], v[2:17], v203, v203 op_sel_hi:[0,0,0]
	v_exp_f32_e64 v26, -v26
	v_exp_f32_e64 v27, -v27
	v_exp_f32_e64 v28, -v28
	v_exp_f32_e64 v29, -v29
	v_add_co_u32_e64 v200, s[42:43], v200, v200
	v_add_co_u32_e64 v200, s[48:49], v200, v200
	v_add_co_u32_e64 v200, s[50:51], v200, v200
	v_add_co_u32_e64 v200, s[56:57], v200, v200
	v_pk_add_f32 v[26:27], v[26:27], v[186:187]
	v_pk_add_f32 v[28:29], v[28:29], v[188:189]
	s_mov_b64 exec, s[42:43]
	v_mul_f32_e32 v228, v228, v26
	s_mov_b64 exec, s[48:49]
	v_mul_f32_e32 v229, v229, v27
	s_mov_b64 exec, s[50:51]
	v_mul_f32_e32 v230, v230, v28
	s_mov_b64 exec, s[56:57]
	v_mul_f32_e32 v231, v231, v29
	s_mov_b64 exec, -1
	s_nop 1
	s_waitcnt vmcnt(0)
	v_mfma_scale_f32_32x32x64_f8f6f4 v[2:17], v[58:65], v[98:105], v[2:17], v203, v203 op_sel_hi:[0,0,0]
	v_exp_f32_e64 v30, -v30
	v_exp_f32_e64 v31, -v31
	v_exp_f32_e64 v32, -v32
	v_exp_f32_e64 v33, -v33
	v_add_co_u32_e64 v200, s[42:43], v200, v200
	v_add_co_u32_e64 v200, s[48:49], v200, v200
	v_add_co_u32_e64 v200, s[50:51], v200, v200
	v_add_co_u32_e64 v200, s[56:57], v200, v200
	v_pk_add_f32 v[30:31], v[30:31], v[190:191]
	v_pk_add_f32 v[32:33], v[32:33], v[192:193]
	s_mov_b64 exec, s[42:43]
	v_mul_f32_e32 v232, v232, v30
	s_mov_b64 exec, s[48:49]
	v_mul_f32_e32 v233, v233, v31
	s_mov_b64 exec, s[50:51]
	v_mul_f32_e32 v234, v234, v32
	s_mov_b64 exec, s[56:57]
	v_mul_f32_e32 v235, v235, v33
	s_mov_b64 exec, -1
	s_nop 1
	s_lshl_b32 s34, s39, 2
	s_add_i32 s34, s34, 2
	s_add_i32 s34, s34, s35
	s_and_b32 s41, s34, 15
	s_add_i32 s54, s34, 1
	s_and_b32 s54, s54, 15
	s_lshl_b32 s55, s41, 8
	s_lshl_b32 s38, s52, 12
	s_add_i32 s55, s55, s38
	v_lshl_add_u32 v236, v194, 2, s55
	ds_read_b32 v200, v236
	s_lshl_b32 s34, s54, 3
	s_add_i32 s34, s34, s52
	s_lshl_b32 s34, s34, 13
	s_add_i32 s34, s34, s53
	buffer_load_dwordx4 v[146:149], v195, s[44:47], s34 offen
	s_or_b32 s42, s34, 0x400
	buffer_load_dwordx4 v[150:153], v195, s[44:47], s42 offen
	s_or_b32 s43, s34, 0x800
	buffer_load_dwordx4 v[154:157], v195, s[44:47], s43 offen
	s_or_b32 s42, s34, 0xc00
	buffer_load_dwordx4 v[158:161], v195, s[44:47], s42 offen
	s_or_b32 s43, s34, 0x1000
	buffer_load_dwordx4 v[138:141], v195, s[44:47], s43 offen
	s_or_b32 s42, s34, 0x1400
	buffer_load_dwordx4 v[142:145], v195, s[44:47], s42 offen
	s_or_b32 s43, s34, 0x1800
	buffer_load_dwordx4 v[130:133], v195, s[44:47], s43 offen
	s_or_b32 s42, s34, 0x1c00
	buffer_load_dwordx4 v[134:137], v195, s[44:47], s42 offen
	s_lshl_b32 s55, s41, 3
	s_add_i32 s55, s55, s52
	s_cmp_lg_u32 s55, s33
	s_cbranch_scc1 .Lq2_nd0_2
	v_cndmask_b32_e64 v2, v2, v198, s[0:1]
	v_cndmask_b32_e64 v3, v3, v198, s[2:3]
	v_cndmask_b32_e64 v4, v4, v198, s[4:5]
	v_cndmask_b32_e64 v5, v5, v198, s[6:7]
	v_cndmask_b32_e64 v6, v6, v198, s[8:9]
	v_cndmask_b32_e64 v7, v7, v198, s[10:11]
	v_cndmask_b32_e64 v8, v8, v198, s[12:13]
	v_cndmask_b32_e64 v9, v9, v198, s[14:15]
	v_cndmask_b32_e64 v10, v10, v198, s[16:17]
	v_cndmask_b32_e64 v11, v11, v198, s[18:19]
	v_cndmask_b32_e64 v12, v12, v198, s[20:21]
	v_cndmask_b32_e64 v13, v13, v198, s[22:23]
	v_cndmask_b32_e64 v14, v14, v198, s[24:25]
	v_cndmask_b32_e64 v15, v15, v198, s[26:27]
	v_cndmask_b32_e64 v16, v16, v198, s[28:29]
	v_cndmask_b32_e64 v17, v17, v198, s[30:31]
.Lq2_nd0_2:
	v_mfma_scale_f32_32x32x64_f8f6f4 v[18:33], v[66:73], v[106:113], 0, v203, v203 op_sel_hi:[0,0,0]
	v_exp_f32_e64 v2, -v2
	v_exp_f32_e64 v3, -v3
	v_exp_f32_e64 v4, -v4
	v_exp_f32_e64 v5, -v5
	s_waitcnt lgkmcnt(0)
	v_add_co_u32_e64 v200, s[42:43], v200, v200
	v_add_co_u32_e64 v200, s[48:49], v200, v200
	v_add_co_u32_e64 v200, s[50:51], v200, v200
	v_add_co_u32_e64 v200, s[56:57], v200, v200
	v_pk_add_f32 v[2:3], v[2:3], v[162:163]
	v_pk_add_f32 v[4:5], v[4:5], v[164:165]
	s_mov_b64 exec, s[42:43]
	v_mul_f32_e32 v204, v204, v2
	s_mov_b64 exec, s[48:49]
	v_mul_f32_e32 v205, v205, v3
	s_mov_b64 exec, s[50:51]
	v_mul_f32_e32 v206, v206, v4
	s_mov_b64 exec, s[56:57]
	v_mul_f32_e32 v207, v207, v5
	s_mov_b64 exec, -1
	s_nop 1
	v_mfma_scale_f32_32x32x64_f8f6f4 v[18:33], v[74:81], v[122:129], v[18:33], v203, v203 op_sel_hi:[0,0,0]
	v_exp_f32_e64 v6, -v6
	v_exp_f32_e64 v7, -v7
	v_exp_f32_e64 v8, -v8
	v_exp_f32_e64 v9, -v9
	v_add_co_u32_e64 v200, s[42:43], v200, v200
	v_add_co_u32_e64 v200, s[48:49], v200, v200
	v_add_co_u32_e64 v200, s[50:51], v200, v200
	v_add_co_u32_e64 v200, s[56:57], v200, v200
	v_pk_add_f32 v[6:7], v[6:7], v[166:167]
	v_pk_add_f32 v[8:9], v[8:9], v[168:169]
	s_mov_b64 exec, s[42:43]
	v_mul_f32_e32 v208, v208, v6
	s_mov_b64 exec, s[48:49]
	v_mul_f32_e32 v209, v209, v7
	s_mov_b64 exec, s[50:51]
	v_mul_f32_e32 v210, v210, v8
	s_mov_b64 exec, s[56:57]
	v_mul_f32_e32 v211, v211, v9
	s_mov_b64 exec, -1
	s_nop 1
	v_mfma_scale_f32_32x32x64_f8f6f4 v[18:33], v[82:89], v[114:121], v[18:33], v203, v203 op_sel_hi:[0,0,0]
	v_exp_f32_e64 v10, -v10
	v_exp_f32_e64 v11, -v11
	v_exp_f32_e64 v12, -v12
	v_exp_f32_e64 v13, -v13
	v_add_co_u32_e64 v200, s[42:43], v200, v200
	v_add_co_u32_e64 v200, s[48:49], v200, v200
	v_add_co_u32_e64 v200, s[50:51], v200, v200
	v_add_co_u32_e64 v200, s[56:57], v200, v200
	v_pk_add_f32 v[10:11], v[10:11], v[170:171]
	v_pk_add_f32 v[12:13], v[12:13], v[172:173]
	s_mov_b64 exec, s[42:43]
	v_mul_f32_e32 v212, v212, v10
	s_mov_b64 exec, s[48:49]
	v_mul_f32_e32 v213, v213, v11
	s_mov_b64 exec, s[50:51]
	v_mul_f32_e32 v214, v214, v12
	s_mov_b64 exec, s[56:57]
	v_mul_f32_e32 v215, v215, v13
	s_mov_b64 exec, -1
	s_nop 1
	v_mfma_scale_f32_32x32x64_f8f6f4 v[18:33], v[90:97], v[98:105], v[18:33], v203, v203 op_sel_hi:[0,0,0]
	v_exp_f32_e64 v14, -v14
	v_exp_f32_e64 v15, -v15
	v_exp_f32_e64 v16, -v16
	v_exp_f32_e64 v17, -v17
	v_add_co_u32_e64 v200, s[42:43], v200, v200
	v_add_co_u32_e64 v200, s[48:49], v200, v200
	v_add_co_u32_e64 v200, s[50:51], v200, v200
	v_add_co_u32_e64 v200, s[56:57], v200, v200
	v_pk_add_f32 v[14:15], v[14:15], v[174:175]
	v_pk_add_f32 v[16:17], v[16:17], v[176:177]
	s_mov_b64 exec, s[42:43]
	v_mul_f32_e32 v216, v216, v14
	s_mov_b64 exec, s[48:49]
	v_mul_f32_e32 v217, v217, v15
	s_mov_b64 exec, s[50:51]
	v_mul_f32_e32 v218, v218, v16
	s_mov_b64 exec, s[56:57]
	v_mul_f32_e32 v219, v219, v17
	s_mov_b64 exec, -1
	s_nop 1
	s_cmp_lg_u32 s55, s40
	s_cbranch_scc1 .Lq2_nd1_2
	s_nop 15
	s_nop 7
	v_cndmask_b32_e64 v18, v18, v199, s[0:1]
	v_cndmask_b32_e64 v19, v19, v199, s[2:3]
	v_cndmask_b32_e64 v20, v20, v199, s[4:5]
	v_cndmask_b32_e64 v21, v21, v199, s[6:7]
	v_cndmask_b32_e64 v22, v22, v199, s[8:9]
	v_cndmask_b32_e64 v23, v23, v199, s[10:11]
	v_cndmask_b32_e64 v24, v24, v199, s[12:13]
	v_cndmask_b32_e64 v25, v25, v199, s[14:15]
	v_cndmask_b32_e64 v26, v26, v199, s[16:17]
	v_cndmask_b32_e64 v27, v27, v199, s[18:19]
	v_cndmask_b32_e64 v28, v28, v199, s[20:21]
	v_cndmask_b32_e64 v29, v29, v199, s[22:23]
	v_cndmask_b32_e64 v30, v30, v199, s[24:25]
	v_cndmask_b32_e64 v31, v31, v199, s[26:27]
	v_cndmask_b32_e64 v32, v32, v199, s[28:29]
	v_cndmask_b32_e64 v33, v33, v199, s[30:31]
.Lq2_nd1_2:
	s_nop 3
	s_waitcnt vmcnt(6)
	v_mfma_scale_f32_32x32x64_f8f6f4 v[2:17], v[34:41], v[146:153], 0, v203, v203 op_sel_hi:[0,0,0]
	v_exp_f32_e64 v18, -v18
	v_exp_f32_e64 v19, -v19
	v_exp_f32_e64 v20, -v20
	v_exp_f32_e64 v21, -v21
	v_add_co_u32_e64 v200, s[42:43], v200, v200
	v_add_co_u32_e64 v200, s[48:49], v200, v200
	v_add_co_u32_e64 v200, s[50:51], v200, v200
	v_add_co_u32_e64 v200, s[56:57], v200, v200
	v_pk_add_f32 v[18:19], v[18:19], v[178:179]
	v_pk_add_f32 v[20:21], v[20:21], v[180:181]
	s_mov_b64 exec, s[42:43]
	v_mul_f32_e32 v220, v220, v18
	s_mov_b64 exec, s[48:49]
	v_mul_f32_e32 v221, v221, v19
	s_mov_b64 exec, s[50:51]
	v_mul_f32_e32 v222, v222, v20
	s_mov_b64 exec, s[56:57]
	v_mul_f32_e32 v223, v223, v21
	s_mov_b64 exec, -1
	s_nop 1
	s_waitcnt vmcnt(4)
	v_mfma_scale_f32_32x32x64_f8f6f4 v[2:17], v[42:49], v[154:161], v[2:17], v203, v203 op_sel_hi:[0,0,0]
	v_exp_f32_e64 v22, -v22
	v_exp_f32_e64 v23, -v23
	v_exp_f32_e64 v24, -v24
	v_exp_f32_e64 v25, -v25
	v_add_co_u32_e64 v200, s[42:43], v200, v200
	v_add_co_u32_e64 v200, s[48:49], v200, v200
	v_add_co_u32_e64 v200, s[50:51], v200, v200
	v_add_co_u32_e64 v200, s[56:57], v200, v200
	v_pk_add_f32 v[22:23], v[22:23], v[182:183]
	v_pk_add_f32 v[24:25], v[24:25], v[184:185]
	s_mov_b64 exec, s[42:43]
	v_mul_f32_e32 v224, v224, v22
	s_mov_b64 exec, s[48:49]
	v_mul_f32_e32 v225, v225, v23
	s_mov_b64 exec, s[50:51]
	v_mul_f32_e32 v226, v226, v24
	s_mov_b64 exec, s[56:57]
	v_mul_f32_e32 v227, v227, v25
	s_mov_b64 exec, -1
	s_nop 1
	s_waitcnt vmcnt(2)
	v_mfma_scale_f32_32x32x64_f8f6f4 v[2:17], v[50:57], v[138:145], v[2:17], v203, v203 op_sel_hi:[0,0,0]
	v_exp_f32_e64 v26, -v26
	v_exp_f32_e64 v27, -v27
	v_exp_f32_e64 v28, -v28
	v_exp_f32_e64 v29, -v29
	v_add_co_u32_e64 v200, s[42:43], v200, v200
	v_add_co_u32_e64 v200, s[48:49], v200, v200
	v_add_co_u32_e64 v200, s[50:51], v200, v200
	v_add_co_u32_e64 v200, s[56:57], v200, v200
	v_pk_add_f32 v[26:27], v[26:27], v[186:187]
	v_pk_add_f32 v[28:29], v[28:29], v[188:189]
	s_mov_b64 exec, s[42:43]
	v_mul_f32_e32 v228, v228, v26
	s_mov_b64 exec, s[48:49]
	v_mul_f32_e32 v229, v229, v27
	s_mov_b64 exec, s[50:51]
	v_mul_f32_e32 v230, v230, v28
	s_mov_b64 exec, s[56:57]
	v_mul_f32_e32 v231, v231, v29
	s_mov_b64 exec, -1
	s_nop 1
	s_waitcnt vmcnt(0)
	v_mfma_scale_f32_32x32x64_f8f6f4 v[2:17], v[58:65], v[130:137], v[2:17], v203, v203 op_sel_hi:[0,0,0]
	v_exp_f32_e64 v30, -v30
	v_exp_f32_e64 v31, -v31
	v_exp_f32_e64 v32, -v32
	v_exp_f32_e64 v33, -v33
	v_add_co_u32_e64 v200, s[42:43], v200, v200
	v_add_co_u32_e64 v200, s[48:49], v200, v200
	v_add_co_u32_e64 v200, s[50:51], v200, v200
	v_add_co_u32_e64 v200, s[56:57], v200, v200
	v_pk_add_f32 v[30:31], v[30:31], v[190:191]
	v_pk_add_f32 v[32:33], v[32:33], v[192:193]
	s_mov_b64 exec, s[42:43]
	v_mul_f32_e32 v232, v232, v30
	s_mov_b64 exec, s[48:49]
	v_mul_f32_e32 v233, v233, v31
	s_mov_b64 exec, s[50:51]
	v_mul_f32_e32 v234, v234, v32
	s_mov_b64 exec, s[56:57]
	v_mul_f32_e32 v235, v235, v33
	s_mov_b64 exec, -1
	s_nop 1
	s_lshl_b32 s34, s39, 2
	s_add_i32 s34, s34, 3
	s_add_i32 s34, s34, s35
	s_and_b32 s41, s34, 15
	s_add_i32 s54, s34, 1
	s_and_b32 s54, s54, 15
	s_lshl_b32 s55, s41, 8
	s_lshl_b32 s38, s52, 12
	s_add_i32 s55, s55, s38
	v_lshl_add_u32 v236, v194, 2, s55
	ds_read_b32 v200, v236
	s_lshl_b32 s34, s54, 3
	s_add_i32 s34, s34, s52
	s_lshl_b32 s34, s34, 13
	s_add_i32 s34, s34, s53
	buffer_load_dwordx4 v[106:109], v195, s[44:47], s34 offen
	s_or_b32 s42, s34, 0x400
	buffer_load_dwordx4 v[110:113], v195, s[44:47], s42 offen
	s_or_b32 s43, s34, 0x800
	buffer_load_dwordx4 v[122:125], v195, s[44:47], s43 offen
	s_or_b32 s42, s34, 0xc00
	buffer_load_dwordx4 v[126:129], v195, s[44:47], s42 offen
	s_or_b32 s43, s34, 0x1000
	buffer_load_dwordx4 v[114:117], v195, s[44:47], s43 offen
	s_or_b32 s42, s34, 0x1400
	buffer_load_dwordx4 v[118:121], v195, s[44:47], s42 offen
	s_or_b32 s43, s34, 0x1800
	buffer_load_dwordx4 v[98:101], v195, s[44:47], s43 offen
	s_or_b32 s42, s34, 0x1c00
	buffer_load_dwordx4 v[102:105], v195, s[44:47], s42 offen
	s_lshl_b32 s55, s41, 3
	s_add_i32 s55, s55, s52
	s_cmp_lg_u32 s55, s33
	s_cbranch_scc1 .Lq2_nd0_3
	v_cndmask_b32_e64 v2, v2, v198, s[0:1]
	v_cndmask_b32_e64 v3, v3, v198, s[2:3]
	v_cndmask_b32_e64 v4, v4, v198, s[4:5]
	v_cndmask_b32_e64 v5, v5, v198, s[6:7]
	v_cndmask_b32_e64 v6, v6, v198, s[8:9]
	v_cndmask_b32_e64 v7, v7, v198, s[10:11]
	v_cndmask_b32_e64 v8, v8, v198, s[12:13]
	v_cndmask_b32_e64 v9, v9, v198, s[14:15]
	v_cndmask_b32_e64 v10, v10, v198, s[16:17]
	v_cndmask_b32_e64 v11, v11, v198, s[18:19]
	v_cndmask_b32_e64 v12, v12, v198, s[20:21]
	v_cndmask_b32_e64 v13, v13, v198, s[22:23]
	v_cndmask_b32_e64 v14, v14, v198, s[24:25]
	v_cndmask_b32_e64 v15, v15, v198, s[26:27]
	v_cndmask_b32_e64 v16, v16, v198, s[28:29]
	v_cndmask_b32_e64 v17, v17, v198, s[30:31]
.Lq2_nd0_3:
	v_mfma_scale_f32_32x32x64_f8f6f4 v[18:33], v[66:73], v[146:153], 0, v203, v203 op_sel_hi:[0,0,0]
	ds_read_b128 v[236:239], v202
	v_exp_f32_e64 v2, -v2
	v_exp_f32_e64 v3, -v3
	v_exp_f32_e64 v4, -v4
	v_exp_f32_e64 v5, -v5
	s_waitcnt lgkmcnt(1)
	v_add_co_u32_e64 v200, s[42:43], v200, v200
	v_add_co_u32_e64 v200, s[48:49], v200, v200
	v_add_co_u32_e64 v200, s[50:51], v200, v200
	v_add_co_u32_e64 v200, s[56:57], v200, v200
	v_pk_add_f32 v[2:3], v[2:3], v[162:163]
	v_pk_add_f32 v[4:5], v[4:5], v[164:165]
	s_mov_b64 exec, s[42:43]
	v_mul_f32_e32 v204, v204, v2
	s_mov_b64 exec, s[48:49]
	v_mul_f32_e32 v205, v205, v3
	s_mov_b64 exec, s[50:51]
	v_mul_f32_e32 v206, v206, v4
	s_mov_b64 exec, s[56:57]
	v_mul_f32_e32 v207, v207, v5
	s_mov_b64 exec, -1
	s_nop 1
	v_log_f32_e32 v2, v204
	v_log_f32_e32 v3, v205
	v_log_f32_e32 v4, v206
	v_log_f32_e32 v5, v207
	s_waitcnt lgkmcnt(0)
	v_fmac_f32_e32 v201, v2, v236
	v_fmac_f32_e32 v201, v3, v237
	v_fmac_f32_e32 v201, v4, v238
	v_fmac_f32_e32 v201, v5, v239
	v_mfma_scale_f32_32x32x64_f8f6f4 v[18:33], v[74:81], v[154:161], v[18:33], v203, v203 op_sel_hi:[0,0,0]
	ds_read_b128 v[236:239], v202 offset:16
	v_exp_f32_e64 v6, -v6
	v_exp_f32_e64 v7, -v7
	v_exp_f32_e64 v8, -v8
	v_exp_f32_e64 v9, -v9
	v_add_co_u32_e64 v200, s[42:43], v200, v200
	v_add_co_u32_e64 v200, s[48:49], v200, v200
	v_add_co_u32_e64 v200, s[50:51], v200, v200
	v_add_co_u32_e64 v200, s[56:57], v200, v200
	v_pk_add_f32 v[6:7], v[6:7], v[166:167]
	v_pk_add_f32 v[8:9], v[8:9], v[168:169]
	s_mov_b64 exec, s[42:43]
	v_mul_f32_e32 v208, v208, v6
	s_mov_b64 exec, s[48:49]
	v_mul_f32_e32 v209, v209, v7
	s_mov_b64 exec, s[50:51]
	v_mul_f32_e32 v210, v210, v8
	s_mov_b64 exec, s[56:57]
	v_mul_f32_e32 v211, v211, v9
	s_mov_b64 exec, -1
	s_nop 1
	v_log_f32_e32 v6, v208
	v_log_f32_e32 v7, v209
	v_log_f32_e32 v8, v210
	v_log_f32_e32 v9, v211
	s_waitcnt lgkmcnt(0)
	v_fmac_f32_e32 v201, v6, v236
	v_fmac_f32_e32 v201, v7, v237
	v_fmac_f32_e32 v201, v8, v238
	v_fmac_f32_e32 v201, v9, v239
	v_mfma_scale_f32_32x32x64_f8f6f4 v[18:33], v[82:89], v[138:145], v[18:33], v203, v203 op_sel_hi:[0,0,0]
	ds_read_b128 v[236:239], v202 offset:32
	v_exp_f32_e64 v10, -v10
	v_exp_f32_e64 v11, -v11
	v_exp_f32_e64 v12, -v12
	v_exp_f32_e64 v13, -v13
	v_add_co_u32_e64 v200, s[42:43], v200, v200
	v_add_co_u32_e64 v200, s[48:49], v200, v200
	v_add_co_u32_e64 v200, s[50:51], v200, v200
	v_add_co_u32_e64 v200, s[56:57], v200, v200
	v_pk_add_f32 v[10:11], v[10:11], v[170:171]
	v_pk_add_f32 v[12:13], v[12:13], v[172:173]
	s_mov_b64 exec, s[42:43]
	v_mul_f32_e32 v212, v212, v10
	s_mov_b64 exec, s[48:49]
	v_mul_f32_e32 v213, v213, v11
	s_mov_b64 exec, s[50:51]
	v_mul_f32_e32 v214, v214, v12
	s_mov_b64 exec, s[56:57]
	v_mul_f32_e32 v215, v215, v13
	s_mov_b64 exec, -1
	s_nop 1
	v_log_f32_e32 v10, v212
	v_log_f32_e32 v11, v213
	v_log_f32_e32 v12, v214
	v_log_f32_e32 v13, v215
	s_waitcnt lgkmcnt(0)
	v_fmac_f32_e32 v201, v10, v236
	v_fmac_f32_e32 v201, v11, v237
	v_fmac_f32_e32 v201, v12, v238
	v_fmac_f32_e32 v201, v13, v239
	v_mfma_scale_f32_32x32x64_f8f6f4 v[18:33], v[90:97], v[130:137], v[18:33], v203, v203 op_sel_hi:[0,0,0]
	ds_read_b128 v[236:239], v202 offset:48
	v_exp_f32_e64 v14, -v14
	v_exp_f32_e64 v15, -v15
	v_exp_f32_e64 v16, -v16
	v_exp_f32_e64 v17, -v17
	v_add_co_u32_e64 v200, s[42:43], v200, v200
	v_add_co_u32_e64 v200, s[48:49], v200, v200
	v_add_co_u32_e64 v200, s[50:51], v200, v200
	v_add_co_u32_e64 v200, s[56:57], v200, v200
	v_pk_add_f32 v[14:15], v[14:15], v[174:175]
	v_pk_add_f32 v[16:17], v[16:17], v[176:177]
	s_mov_b64 exec, s[42:43]
	v_mul_f32_e32 v216, v216, v14
	s_mov_b64 exec, s[48:49]
	v_mul_f32_e32 v217, v217, v15
	s_mov_b64 exec, s[50:51]
	v_mul_f32_e32 v218, v218, v16
	s_mov_b64 exec, s[56:57]
	v_mul_f32_e32 v219, v219, v17
	s_mov_b64 exec, -1
	s_nop 1
	v_log_f32_e32 v14, v216
	v_log_f32_e32 v15, v217
	v_log_f32_e32 v16, v218
	v_log_f32_e32 v17, v219
	s_waitcnt lgkmcnt(0)
	v_fmac_f32_e32 v201, v14, v236
	v_fmac_f32_e32 v201, v15, v237
	v_fmac_f32_e32 v201, v16, v238
	v_fmac_f32_e32 v201, v17, v239
	s_cmp_lg_u32 s55, s40
	s_cbranch_scc1 .Lq2_nd1_3
	s_nop 15
	s_nop 7
	v_cndmask_b32_e64 v18, v18, v199, s[0:1]
	v_cndmask_b32_e64 v19, v19, v199, s[2:3]
	v_cndmask_b32_e64 v20, v20, v199, s[4:5]
	v_cndmask_b32_e64 v21, v21, v199, s[6:7]
	v_cndmask_b32_e64 v22, v22, v199, s[8:9]
	v_cndmask_b32_e64 v23, v23, v199, s[10:11]
	v_cndmask_b32_e64 v24, v24, v199, s[12:13]
	v_cndmask_b32_e64 v25, v25, v199, s[14:15]
	v_cndmask_b32_e64 v26, v26, v199, s[16:17]
	v_cndmask_b32_e64 v27, v27, v199, s[18:19]
	v_cndmask_b32_e64 v28, v28, v199, s[20:21]
	v_cndmask_b32_e64 v29, v29, v199, s[22:23]
	v_cndmask_b32_e64 v30, v30, v199, s[24:25]
	v_cndmask_b32_e64 v31, v31, v199, s[26:27]
	v_cndmask_b32_e64 v32, v32, v199, s[28:29]
	v_cndmask_b32_e64 v33, v33, v199, s[30:31]
.Lq2_nd1_3:
	s_nop 3
	s_waitcnt vmcnt(6)
	v_mfma_scale_f32_32x32x64_f8f6f4 v[2:17], v[34:41], v[106:113], 0, v203, v203 op_sel_hi:[0,0,0]
	ds_read_b128 v[236:239], v202 offset:64
	v_exp_f32_e64 v18, -v18
	v_exp_f32_e64 v19, -v19
	v_exp_f32_e64 v20, -v20
	v_exp_f32_e64 v21, -v21
	v_add_co_u32_e64 v200, s[42:43], v200, v200
	v_add_co_u32_e64 v200, s[48:49], v200, v200
	v_add_co_u32_e64 v200, s[50:51], v200, v200
	v_add_co_u32_e64 v200, s[56:57], v200, v200
	v_pk_add_f32 v[18:19], v[18:19], v[178:179]
	v_pk_add_f32 v[20:21], v[20:21], v[180:181]
	s_mov_b64 exec, s[42:43]
	v_mul_f32_e32 v220, v220, v18
	s_mov_b64 exec, s[48:49]
	v_mul_f32_e32 v221, v221, v19
	s_mov_b64 exec, s[50:51]
	v_mul_f32_e32 v222, v222, v20
	s_mov_b64 exec, s[56:57]
	v_mul_f32_e32 v223, v223, v21
	s_mov_b64 exec, -1
	s_nop 1
	v_log_f32_e32 v18, v220
	v_log_f32_e32 v19, v221
	v_log_f32_e32 v20, v222
	v_log_f32_e32 v21, v223
	s_waitcnt lgkmcnt(0)
	v_fmac_f32_e32 v201, v18, v236
	v_fmac_f32_e32 v201, v19, v237
	v_fmac_f32_e32 v201, v20, v238
	v_fmac_f32_e32 v201, v21, v239
	s_waitcnt vmcnt(4)
	v_mfma_scale_f32_32x32x64_f8f6f4 v[2:17], v[42:49], v[122:129], v[2:17], v203, v203 op_sel_hi:[0,0,0]
	ds_read_b128 v[236:239], v202 offset:80
	v_exp_f32_e64 v22, -v22
	v_exp_f32_e64 v23, -v23
	v_exp_f32_e64 v24, -v24
	v_exp_f32_e64 v25, -v25
	v_add_co_u32_e64 v200, s[42:43], v200, v200
	v_add_co_u32_e64 v200, s[48:49], v200, v200
	v_add_co_u32_e64 v200, s[50:51], v200, v200
	v_add_co_u32_e64 v200, s[56:57], v200, v200
	v_pk_add_f32 v[22:23], v[22:23], v[182:183]
	v_pk_add_f32 v[24:25], v[24:25], v[184:185]
	s_mov_b64 exec, s[42:43]
	v_mul_f32_e32 v224, v224, v22
	s_mov_b64 exec, s[48:49]
	v_mul_f32_e32 v225, v225, v23
	s_mov_b64 exec, s[50:51]
	v_mul_f32_e32 v226, v226, v24
	s_mov_b64 exec, s[56:57]
	v_mul_f32_e32 v227, v227, v25
	s_mov_b64 exec, -1
	s_nop 1
	v_log_f32_e32 v22, v224
	v_log_f32_e32 v23, v225
	v_log_f32_e32 v24, v226
	v_log_f32_e32 v25, v227
	s_waitcnt lgkmcnt(0)
	v_fmac_f32_e32 v201, v22, v236
	v_fmac_f32_e32 v201, v23, v237
	v_fmac_f32_e32 v201, v24, v238
	v_fmac_f32_e32 v201, v25, v239
	s_waitcnt vmcnt(2)
	v_mfma_scale_f32_32x32x64_f8f6f4 v[2:17], v[50:57], v[114:121], v[2:17], v203, v203 op_sel_hi:[0,0,0]
	ds_read_b128 v[236:239], v202 offset:96
	v_exp_f32_e64 v26, -v26
	v_exp_f32_e64 v27, -v27
	v_exp_f32_e64 v28, -v28
	v_exp_f32_e64 v29, -v29
	v_add_co_u32_e64 v200, s[42:43], v200, v200
	v_add_co_u32_e64 v200, s[48:49], v200, v200
	v_add_co_u32_e64 v200, s[50:51], v200, v200
	v_add_co_u32_e64 v200, s[56:57], v200, v200
	v_pk_add_f32 v[26:27], v[26:27], v[186:187]
	v_pk_add_f32 v[28:29], v[28:29], v[188:189]
	s_mov_b64 exec, s[42:43]
	v_mul_f32_e32 v228, v228, v26
	s_mov_b64 exec, s[48:49]
	v_mul_f32_e32 v229, v229, v27
	s_mov_b64 exec, s[50:51]
	v_mul_f32_e32 v230, v230, v28
	s_mov_b64 exec, s[56:57]
	v_mul_f32_e32 v231, v231, v29
	s_mov_b64 exec, -1
	s_nop 1
	v_log_f32_e32 v26, v228
	v_log_f32_e32 v27, v229
	v_log_f32_e32 v28, v230
	v_log_f32_e32 v29, v231
	s_waitcnt lgkmcnt(0)
	v_fmac_f32_e32 v201, v26, v236
	v_fmac_f32_e32 v201, v27, v237
	v_fmac_f32_e32 v201, v28, v238
	v_fmac_f32_e32 v201, v29, v239
	s_waitcnt vmcnt(0)
	v_mfma_scale_f32_32x32x64_f8f6f4 v[2:17], v[58:65], v[98:105], v[2:17], v203, v203 op_sel_hi:[0,0,0]
	ds_read_b128 v[236:239], v202 offset:112
	v_exp_f32_e64 v30, -v30
	v_exp_f32_e64 v31, -v31
	v_exp_f32_e64 v32, -v32
	v_exp_f32_e64 v33, -v33
	v_add_co_u32_e64 v200, s[42:43], v200, v200
	v_add_co_u32_e64 v200, s[48:49], v200, v200
	v_add_co_u32_e64 v200, s[50:51], v200, v200
	v_add_co_u32_e64 v200, s[56:57], v200, v200
	v_pk_add_f32 v[30:31], v[30:31], v[190:191]
	v_pk_add_f32 v[32:33], v[32:33], v[192:193]
	s_mov_b64 exec, s[42:43]
	v_mul_f32_e32 v232, v232, v30
	s_mov_b64 exec, s[48:49]
	v_mul_f32_e32 v233, v233, v31
	s_mov_b64 exec, s[50:51]
	v_mul_f32_e32 v234, v234, v32
	s_mov_b64 exec, s[56:57]
	v_mul_f32_e32 v235, v235, v33
	s_mov_b64 exec, -1
	s_nop 1
	v_log_f32_e32 v30, v232
	v_log_f32_e32 v31, v233
	v_log_f32_e32 v32, v234
	v_log_f32_e32 v33, v235
	s_waitcnt lgkmcnt(0)
	v_fmac_f32_e32 v201, v30, v236
	v_fmac_f32_e32 v201, v31, v237
	v_fmac_f32_e32 v201, v32, v238
	v_fmac_f32_e32 v201, v33, v239
	s_add_i32 s39, s39, 1
	s_cmp_lt_u32 s39, 4
	s_cbranch_scc1 .Lq2_loop
